# speedup vs baseline: 1.0038x; 1.0038x over previous
.LBB1_70:
	s_or_b64 exec, exec, s[4:5]
	v_lshrrev_b32_e32 v7, 1, v0
	v_lshlrev_b32_e32 v1, 2, v7
	s_waitcnt lgkmcnt(0)
	s_barrier
	s_and_saveexec_b64 s[52:53], vcc
	s_cbranch_execz .LBB1_99
	v_not_b32_e32 v1, v0
	v_add_u32_e32 v2, s33, v1
	s_movk_i32 s4, 0x2a00
	s_movk_i32 s6, 0x29ff
	v_cmp_gt_u32_e64 s[4:5], s4, v2
	v_cmp_lt_u32_e32 vcc, s6, v2
	v_mov_b32_e32 v1, v0
	s_and_saveexec_b64 s[6:7], vcc
	s_cbranch_execz .LBB1_96
	s_add_i32 s8, s36, s38
	s_add_i32 s8, s8, s39
	s_add_i32 s8, s8, s40
	s_add_i32 s8, s8, s41
	s_add_i32 s8, s8, s42
	s_add_i32 s8, s8, s43
	s_add_i32 s8, s8, s37
	v_add_u32_e32 v1, s8, v0
	v_and_b32_e32 v3, 0xfffffe00, v2
	v_add_u32_e32 v3, v1, v3
	v_cmp_ge_i32_e32 vcc, v3, v1
	s_mov_b64 s[10:11], -1
	v_mov_b32_e32 v1, v0
	s_and_saveexec_b64 s[8:9], vcc
	s_cbranch_execz .LBB1_95
	v_lshrrev_b32_e32 v4, 9, v2
	v_add_u32_e32 v2, -1, v4
	v_or_b32_e32 v1, 0x200, v0
	v_lshrrev_b32_e32 v3, 1, v2
	s_mov_b32 s15, 0
	v_add_u32_e32 v5, 1, v3
	v_cmp_lt_u32_e32 vcc, 5, v2
	v_mov_b32_e32 v8, 0
	v_mov_b64_e32 v[2:3], v[0:1]
	s_and_saveexec_b64 s[10:11], vcc
	s_cbranch_execz .LBB1_91
	s_add_i32 s16, s34, 0x400
	s_add_i32 s18, s34, 0x800
	s_add_i32 s20, s34, 0xc00
	v_mov_b32_e32 v2, 0x2000
	v_and_b32_e32 v6, -4, v5
	s_mov_b32 s17, s16
	s_mov_b32 s19, s18
	s_mov_b32 s21, s20
	v_lshl_or_b32 v7, v0, 3, v2
	s_mov_b64 s[12:13], 0
	v_mov_b64_e32 v[2:3], v[0:1]

.LBB1_99:
	s_or_b64 exec, exec, s[52:53]
	v_lshrrev_b32_e32 v7, 1, v0
	v_lshlrev_b32_e32 v1, 2, v7
	v_lshlrev_b32_e32 v73, 3, v7
	ds_read_b32 v6, v73 offset:5248
	s_movk_i32 s4, 0x1fe
	v_cmp_gt_u32_e64 s[4:5], s4, v0
	v_mov_b32_e32 v9, s33
	s_and_saveexec_b64 s[6:7], s[4:5]
	ds_read_b32 v9, v73 offset:5256
	s_or_b64 exec, exec, s[6:7]
	v_and_b32_e32 v8, 1, v0
	s_waitcnt lgkmcnt(0)
	v_add_u32_e32 v10, v6, v8
	v_add_u32_e32 v2, 6, v10
	v_mov_b32_e32 v5, 0
	v_cmp_lt_i32_e64 s[4:5], v2, v9
	v_mov_b32_e32 v4, v5
	v_mov_b32_e32 v3, v5
	v_mov_b32_e32 v2, v5
	s_and_saveexec_b64 s[6:7], s[4:5]
	s_cbranch_execz .LBB1_76
	v_mov_b32_e32 v2, 0x2004
	v_lshl_add_u32 v11, v10, 3, v2
	v_mov_b32_e32 v2, 0
	s_mov_b64 s[8:9], 0
	v_mov_b32_e32 v3, v2
	v_mov_b32_e32 v4, v2
	v_mov_b32_e32 v5, v2
